# combine phases and MoE-down-1 reuse the expert table the preceding phase left in LDS (no counter reload / serial prefix / extra barrier)
# baseline (speedup 1.0000x reference)
.LBB0_1169:
	s_load_dwordx4 s[0:3], s[8:9], 0x138
	s_waitcnt lgkmcnt(0)
	s_mov_b64 s[4:5], s[0:1]
	s_cmp_lt_i32 s4, 9
	s_cselect_b64 s[0:1], -1, 0
	s_cmp_gt_i32 s5, 8
	s_cselect_b64 s[2:3], -1, 0
	s_and_b64 s[0:1], s[0:1], s[2:3]
	s_andn2_b64 vcc, exec, s[0:1]
	s_cbranch_vccnz .LBB0_1234
	s_mov_b64 s[4:5], s[8:9]
	s_waitcnt vmcnt(0)
	v_mbcnt_lo_u32_b32 v8, -1, 0
	v_mbcnt_hi_u32_b32 v8, -1, v8
	s_load_dword s14, s[8:9], 0x148
	s_load_dwordx2 s[10:11], s[4:5], 0x130
	v_add_u32_e32 v0, s33, v8
	s_add_u32 s2, s8, 0x148
	s_addc_u32 s3, s9, 0
	v_cmp_gt_i32_e32 vcc, 32, v0
	s_waitcnt lgkmcnt(0)
	s_barrier
	v_cmp_eq_u32_e64 s[0:1], 0, v0
	s_mov_b64 s[6:7], exec

.LBB0_2023:
	s_load_dwordx2 s[4:5], s[2:3], 0x130
	v_cmp_gt_i32_e32 vcc, 32, v160
	s_waitcnt vmcnt(0) lgkmcnt(0)
	s_barrier
	v_cmp_eq_u32_e32 vcc, 0, v160
	s_mov_b64 s[6:7], exec

.LBB0_2196:
	s_and_b64 vcc, exec, s[2:3]
	s_cbranch_vccz .LBB0_2262
	v_readlane_b32 s4, v243, 7
	v_readlane_b32 s5, v243, 8
	s_load_dwordx4 s[0:3], s[4:5], 0x138
	s_waitcnt lgkmcnt(0)
	s_mov_b64 s[4:5], s[0:1]
	s_cmp_lt_i32 s4, 17
	s_cselect_b64 s[0:1], -1, 0
	s_cmp_gt_i32 s5, 16
	s_cselect_b64 s[2:3], -1, 0
	s_and_b64 s[0:1], s[0:1], s[2:3]
	s_andn2_b64 vcc, exec, s[0:1]
	s_cbranch_vccnz .LBB0_2262
	v_readlane_b32 s0, v243, 7
	v_readlane_b32 s1, v243, 8
	s_mov_b64 s[6:7], s[0:1]
	s_waitcnt vmcnt(0)
	v_mbcnt_lo_u32_b32 v8, -1, 0
	v_mbcnt_hi_u32_b32 v8, -1, v8
	s_load_dword s12, s[0:1], 0x148
	s_load_dwordx2 s[4:5], s[6:7], 0x130
	v_add_u32_e32 v0, s33, v8
	s_add_u32 s2, s0, 0x148
	s_addc_u32 s3, s1, 0
	v_cmp_gt_i32_e32 vcc, 32, v0
	s_waitcnt lgkmcnt(0)
	s_barrier
	v_cmp_eq_u32_e64 s[0:1], 0, v0
	s_mov_b64 s[8:9], exec
